# all 69 inner loop heads aligned to 64 bytes (plus N1 reductions via DPP)
# baseline (speedup 1.0000x reference)
; #define GAS __attribute__((address_space(1)))
; #define MODW_LD(W, j0) do { _Pragma("unroll") for (int q = 0; q < 4; ++q) W[q] = *(const GAS f32x4*)(wp + (size_t)(((j0) + q) & 63) * 16 * 6144); } while (0)
; #define MODW_USE(W, j0) do { _Pragma("unroll") for (int q = 0; q < 4; ++q) { const int k = kg + 16 * ((j0) + q); _Pragma("unroll") for (int r = 0; r < 17; ++r) acc[r] += W[q] * sc[r * 1024 + k]; asm volatile("" ::: "memory"); } } while (0)
; __device__ __forceinline__ void p0_prologue(const Frame& F0) {
;     ...
;         for (int item = blockIdx.x; item < 256; item += F.G) {
;             const int L = item >> 6, n0 = (item & 63) * 96;
;             const int kg = F.tid / 24, cq = F.tid % 24;
;             f32x4 acc[17];
; #pragma unroll
;             for (int r = 0; r < 17; ++r) acc[r] = (f32x4){0.f, 0.f, 0.f, 0.f};
;             if (kg < 16) {
;                 const GAS float* wp = (const GAS float*)(inp(F, I_ADAW) + ((size_t)L * 1024 + kg) * 6144 + n0 + 4 * cq);
;                 f32x4 wa[4], wb[4];
;     ...
;                 MODW_LD(wa, 0);
; #pragma unroll 1
;                 for (int j = 0; j < 64; j += 8) { MODW_LD(wb, j + 4); MODW_USE(wa, j); MODW_LD(wa, j + 8); MODW_USE(wb, j + 4); }
.LBB0_11:
	s_and_b32 s39, s38, 63
	v_mov_b32_e32 v5, 0
	s_ashr_i32 s18, s38, 6
	s_mulk_i32 s39, 0x60
	v_mov_b32_e32 v4, v5
	v_mov_b32_e32 v3, v5
	v_mov_b32_e32 v2, v5
	v_mov_b32_e32 v9, v5
	v_mov_b32_e32 v8, v5
	v_mov_b32_e32 v7, v5
	v_mov_b32_e32 v6, v5
	v_mov_b32_e32 v25, v5
	v_mov_b32_e32 v24, v5
	v_mov_b32_e32 v23, v5
	v_mov_b32_e32 v22, v5
	v_mov_b32_e32 v13, v5
	v_mov_b32_e32 v12, v5
	v_mov_b32_e32 v11, v5
	v_mov_b32_e32 v10, v5
	v_mov_b32_e32 v85, v5
	v_mov_b32_e32 v84, v5
	v_mov_b32_e32 v83, v5
	v_mov_b32_e32 v82, v5
	v_mov_b32_e32 v65, v5
	v_mov_b32_e32 v64, v5
	v_mov_b32_e32 v63, v5
	v_mov_b32_e32 v62, v5
	v_mov_b32_e32 v81, v5
	v_mov_b32_e32 v80, v5
	v_mov_b32_e32 v79, v5
	v_mov_b32_e32 v78, v5
	v_mov_b32_e32 v61, v5
	v_mov_b32_e32 v60, v5
	v_mov_b32_e32 v59, v5
	v_mov_b32_e32 v58, v5
	v_mov_b32_e32 v77, v5
	v_mov_b32_e32 v76, v5
	v_mov_b32_e32 v75, v5
	v_mov_b32_e32 v74, v5
	v_mov_b32_e32 v57, v5
	v_mov_b32_e32 v56, v5
	v_mov_b32_e32 v55, v5
	v_mov_b32_e32 v54, v5
	v_mov_b32_e32 v73, v5
	v_mov_b32_e32 v72, v5
	v_mov_b32_e32 v71, v5
	v_mov_b32_e32 v70, v5
	v_mov_b32_e32 v53, v5
	v_mov_b32_e32 v52, v5
	v_mov_b32_e32 v51, v5
	v_mov_b32_e32 v50, v5
	v_mov_b32_e32 v69, v5
	v_mov_b32_e32 v68, v5
	v_mov_b32_e32 v67, v5
	v_mov_b32_e32 v66, v5
	v_mov_b32_e32 v21, v5
	v_mov_b32_e32 v20, v5
	v_mov_b32_e32 v19, v5
	v_mov_b32_e32 v18, v5
	v_mov_b32_e32 v33, v5
	v_mov_b32_e32 v32, v5
	v_mov_b32_e32 v31, v5
	v_mov_b32_e32 v30, v5
	v_mov_b32_e32 v17, v5
	v_mov_b32_e32 v16, v5
	v_mov_b32_e32 v15, v5
	v_mov_b32_e32 v14, v5
	v_mov_b32_e32 v29, v5
	v_mov_b32_e32 v28, v5
	v_mov_b32_e32 v27, v5
	v_mov_b32_e32 v26, v5
	s_and_saveexec_b64 s[20:21], s[0:1]
	s_cbranch_execz .LBB0_14
	v_mov_b32_e32 v2, s28
	ds_read_b64 v[2:3], v2
	s_ashr_i32 s19, s18, 31
	s_lshl_b64 s[2:3], s[18:19], 10
	v_lshl_add_u64 v[4:5], s[2:3], 0, v[104:105]
	s_lshl_b32 s12, s39, 2
	s_waitcnt lgkmcnt(0)
	v_readfirstlane_b32 s8, v2
	v_readfirstlane_b32 s9, v3
	v_mov_b32_e32 v26, 0
	v_mov_b32_e32 v2, s8
	v_mov_b32_e32 v3, s9
	v_mad_u64_u32 v[2:3], s[2:3], v4, s22, v[2:3]
	v_mad_i32_i24 v3, v5, s22, v3
	v_lshl_add_u64 v[2:3], v[2:3], 0, s[12:13]
	v_lshl_add_u64 v[108:109], v[106:107], 2, v[2:3]
	v_add_co_u32_e32 v2, vcc, s29, v108
	s_mov_b32 s2, -8
	s_nop 0
	v_addc_co_u32_e32 v3, vcc, 0, v109, vcc
	v_add_co_u32_e32 v4, vcc, 0xc0000, v108
	v_mov_b32_e32 v27, v26
	s_nop 0
	v_addc_co_u32_e32 v5, vcc, 0, v109, vcc
	v_add_co_u32_e32 v6, vcc, 0x120000, v108
	v_mov_b32_e32 v28, v26
	s_nop 0
	v_addc_co_u32_e32 v7, vcc, 0, v109, vcc
	global_load_dwordx4 v[42:45], v[4:5], off nt
	global_load_dwordx4 v[34:37], v[6:7], off nt
	global_load_dwordx4 v[46:49], v[2:3], off nt
	global_load_dwordx4 v[38:41], v[108:109], off nt
	v_mov_b32_e32 v29, v26
	v_mov_b32_e32 v14, v26
	v_mov_b32_e32 v15, v26
	v_mov_b32_e32 v16, v26
	v_mov_b32_e32 v17, v26
	v_mov_b32_e32 v30, v26
	v_mov_b32_e32 v31, v26
	v_mov_b32_e32 v32, v26
	v_mov_b32_e32 v33, v26
	v_mov_b32_e32 v18, v26
	v_mov_b32_e32 v19, v26
	v_mov_b32_e32 v20, v26
	v_mov_b32_e32 v21, v26
	v_mov_b32_e32 v66, v26
	v_mov_b32_e32 v67, v26
	v_mov_b32_e32 v68, v26
	v_mov_b32_e32 v69, v26
	v_mov_b32_e32 v50, v26
	v_mov_b32_e32 v51, v26
	v_mov_b32_e32 v52, v26
	v_mov_b32_e32 v53, v26
	v_mov_b32_e32 v70, v26
	v_mov_b32_e32 v71, v26
	v_mov_b32_e32 v72, v26
	v_mov_b32_e32 v73, v26
	v_mov_b32_e32 v54, v26
	v_mov_b32_e32 v55, v26
	v_mov_b32_e32 v56, v26
	v_mov_b32_e32 v57, v26
	v_mov_b32_e32 v74, v26
	v_mov_b32_e32 v75, v26
	v_mov_b32_e32 v76, v26
	v_mov_b32_e32 v77, v26
	v_mov_b32_e32 v58, v26
	v_mov_b32_e32 v59, v26
	v_mov_b32_e32 v60, v26
	v_mov_b32_e32 v61, v26
	v_mov_b32_e32 v78, v26
	v_mov_b32_e32 v79, v26
	v_mov_b32_e32 v80, v26
	v_mov_b32_e32 v81, v26
	v_mov_b32_e32 v62, v26
	v_mov_b32_e32 v63, v26
	v_mov_b32_e32 v64, v26
	v_mov_b32_e32 v65, v26
	v_mov_b32_e32 v82, v26
	v_mov_b32_e32 v83, v26
	v_mov_b32_e32 v84, v26
	v_mov_b32_e32 v85, v26
	v_mov_b32_e32 v10, v26
	v_mov_b32_e32 v11, v26
	v_mov_b32_e32 v12, v26
	v_mov_b32_e32 v13, v26
	v_mov_b32_e32 v22, v26
	v_mov_b32_e32 v23, v26
	v_mov_b32_e32 v24, v26
	v_mov_b32_e32 v25, v26
	v_mov_b32_e32 v6, v26
	v_mov_b32_e32 v7, v26
	v_mov_b32_e32 v8, v26
	v_mov_b32_e32 v9, v26
	v_mov_b32_e32 v2, v26
	v_mov_b32_e32 v3, v26
	v_mov_b32_e32 v4, v26
	v_mov_b32_e32 v5, v26
	v_mov_b32_e32 v131, v1
	v_lshl_add_u64 v[110:111], v[108:109], 0, s[14:15]
	.p2align 6

; #define LAS __attribute__((address_space(3)))
; __device__ __forceinline__ void p0_prologue(const Frame& F0) {
;     ...
; #pragma unroll
;             for (int batch = 0; batch < 2; ++batch) {
;                 const int r0 = batch * 9, nr = batch ? 8 : 9;
;                 if (kg < 16) {
; #pragma unroll
;                     for (int r = 0; r < 9; ++r) if (r0 + r < 17) *(LAS f32x4*)(P + kg * 864 + r * 96 + 4 * cq) = acc[r0 + r < 17 ? r0 + r : 0];
;                 }
;                 __syncthreads();
;                 for (int o = F.tid; o < nr * 96; o += 512) { float s = 0.f;
; #pragma unroll
;                     for (int g = 0; g < 16; ++g) s += P[g * 864 + o];
;                     const int r = r0 + o / 96, n = n0 + o % 96; mod[((size_t)L * 17 + r) * 6144 + n] = s + inp(F, I_ADAB)[L * 6144 + n]; }
.LBB0_16:
	s_or_b64 exec, exec, s[2:3]
	s_mul_i32 s2, s18, 17
	s_mul_i32 s12, s18, 0x1800
	s_ashr_i32 s3, s2, 31
	s_waitcnt lgkmcnt(0)
	s_barrier
	s_and_saveexec_b64 s[8:9], s[4:5]
	s_cbranch_execz .LBB0_19
	s_waitcnt vmcnt(0)
	v_mov_b32_e32 v34, s36
	ds_read_b64 v[34:35], v34
	s_mov_b64 s[10:11], 0
	v_mov_b32_e32 v36, v102
	.p2align 6

; __device__ __forceinline__ void p0_prologue(const Frame& F0) {
;     ...
;                 __syncthreads();
;                 for (int o = F.tid; o < nr * 96; o += 512) { float s = 0.f;
; #pragma unroll
;                     for (int g = 0; g < 16; ++g) s += P[g * 864 + o];
;                     const int r = r0 + o / 96, n = n0 + o % 96; mod[((size_t)L * 17 + r) * 6144 + n] = s + inp(F, I_ADAB)[L * 6144 + n]; }
;                 __syncthreads();
.LBB0_21:
	s_or_b64 exec, exec, s[8:9]
	s_waitcnt lgkmcnt(0)
	s_barrier
	s_and_saveexec_b64 s[8:9], s[6:7]
	s_cbranch_execz .LBB0_10
	v_mov_b32_e32 v2, s36
	ds_read_b64 v[2:3], v2
	s_mov_b64 s[10:11], 0
	v_mov_b32_e32 v4, v102
	.p2align 6

; __device__ __forceinline__ void p0_prologue(const Frame& F0) {
;     ...
;         for (int idx = F.tid; idx < 1024; idx += 512) {
;             const int pos = idx >> 4, i = idx & 15;
;             double f = 1.0; for (int q = 0; q < i; ++q) f *= 0.56234132519034908;
.LBB0_28:
	v_mov_b64_e32 v[2:3], 1.0
	s_and_saveexec_b64 s[34:35], vcc
	s_cbranch_execz .LBB0_27
	s_mov_b64 s[16:17], 0
	v_mov_b64_e32 v[2:3], 1.0
	v_mov_b32_e32 v6, v1
	.p2align 6

; __device__ __forceinline__ void p0_prologue(const Frame& F0) {
;     ...
;         for (int it = gw; it < NITEMS; it += NGW) {
;             if (it >= NSMALL) break;
;             int r = it; const int j = r >= NSMALL / 2 ? 1 : 0; r -= j * (NSMALL / 2);
;             if (r < I_AIN) { p0_transpose_item(inp(F, I_AWIN) + (size_t)j * 1024 * 1536, 1536, (bf16_t*)(ws + WS_WAIN + (size_t)j * 1536 * 1024), RM_AIN, scr, r, F.lane, true); continue; } r -= I_AIN;
;             if (r < I_SQ) { p0_transpose_item(inp(F, I_AWOUT) + (size_t)j * 1024 * 1024, 1024, (bf16_t*)(ws + WS_WAOUT + (size_t)j * 1024 * 1024), RM_P8, scr, r, F.lane, true); continue; } r -= I_SQ;
;             if (r < I_CIN) { p0_transpose_item(inp(F, I_CWIN) + (size_t)j * 1024 * 3072, 3072, (bf16_t*)(ws + WS_WCIN) + (size_t)j * 3072 * 1024, RM_CIN, scr, r, F.lane); continue; } r -= I_CIN;
;             p0_transpose_item(inp(F, I_CWOUT) + (size_t)j * 1024 * 1024, 1024, (bf16_t*)(ws + WS_WCOUT) + (size_t)j * 1024 * 1024, RM_P8, scr, r, F.lane);
;         }
.LBB0_49:
	s_add_i32 s43, s43, s15
	s_add_i32 s19, s19, s20
	s_cmpk_lt_i32 s43, 0x1a00
	s_cbranch_scc0 .LBB0_62
	.p2align 6

; #define GAS __attribute__((address_space(1)))
; #define LAS __attribute__((address_space(3)))
; __device__ __forceinline__ void titem_store(const TItem& T, int lane, const f32x4 (&v)[8], LAS float* scr) {
;     ...
;     for (int j = 0; j < 4; ++j) { const int n = (lane >> 3) + 8 * j; const LAS float* s = scr + (8 * c) * 33 + n;
;         if (T.f8) { u32x2 o; o.x = pg8::pack4_fp8(s[0 * 33] * pg8::SC_W, s[1 * 33] * pg8::SC_W, s[2 * 33] * pg8::SC_W, s[3 * 33] * pg8::SC_W); o.y = pg8::pack4_fp8(s[4 * 33] * pg8::SC_W, s[5 * 33] * pg8::SC_W, s[6 * 33] * pg8::SC_W, s[7 * 33] * pg8::SC_W);
;             *(GAS u32x2*)((unsigned char*)T.WT + (size_t)row_map(T.mode, n0, n) * 1024 + k0 + 8 * c) = o; }
; __device__ __forceinline__ void moe_convert_run(Frame& F, int L, int first, int end, int stride, LAS float* scr) {
;     ...
;     for (int r = first; r < end; r += stride) {
;         const TItem T = nT; f32x4 v[8];
; #pragma unroll
;         for (int i = 0; i < 8; ++i) v[i] = nv[i];
;         if (r + stride < end) { nT = moe_item(F, L, r + stride); titem_load(nT, F.lane, nv); }
;         titem_store(T, F.lane, v, scr);
;     }
.LBB0_76:
	s_waitcnt lgkmcnt(3)
	v_mul_f32_e32 v40, 0x43800000, v40
	v_mul_f32_e32 v41, 0x43800000, v41
	s_waitcnt lgkmcnt(2)
	v_mul_f32_e32 v43, 0x43800000, v38
	v_med3_f32 v40, v40, s23, v77
	v_med3_f32 v41, v41, s23, v77
	v_mov_b32_e32 v38, 0
	v_cvt_pk_fp8_f32 v38, v40, v41
	v_mul_f32_e32 v39, 0x43800000, v39
	v_med3_f32 v40, v43, s23, v77
	v_med3_f32 v39, v39, s23, v77
	s_waitcnt lgkmcnt(1)
	v_mul_f32_e32 v36, 0x43800000, v36
	v_mul_f32_e32 v37, 0x43800000, v37
	v_cvt_pk_fp8_f32 v38, v40, v39 op_sel:[0,0,1]
	v_med3_f32 v36, v36, s23, v77
	v_med3_f32 v37, v37, s23, v77
	v_mov_b32_e32 v39, 0
	v_cvt_pk_fp8_f32 v39, v36, v37
	s_waitcnt lgkmcnt(0)
	v_mul_f32_e32 v34, 0x43800000, v34
	v_mul_f32_e32 v35, 0x43800000, v35
	v_med3_f32 v34, v34, s23, v77
	v_med3_f32 v35, v35, s23, v77
	v_cvt_pk_fp8_f32 v39, v34, v35 op_sel:[0,0,1]
	v_or_b32_e32 v34, v42, v75
	v_ashrrev_i32_e32 v35, 31, v34
	v_lshlrev_b64 v[34:35], 10, v[34:35]
	v_lshl_add_u64 v[34:35], s[0:1], 0, v[34:35]
	v_lshl_add_u64 v[34:35], v[34:35], 0, s[6:7]
	v_lshl_add_u64 v[34:35], v[34:35], 0, v[68:69]
	global_store_dwordx2 v[34:35], v[38:39], off nt
	s_waitcnt lgkmcnt(0)
	s_waitcnt vmcnt(4)
	v_mov_b64_e32 v[36:37], v[32:33]
	v_mov_b64_e32 v[44:45], v[28:29]
	v_mov_b64_e32 v[40:41], v[24:25]
	v_mov_b64_e32 v[48:49], v[20:21]
	v_mov_b64_e32 v[52:53], v[16:17]
	v_mov_b64_e32 v[56:57], v[12:13]
	v_mov_b64_e32 v[60:61], v[8:9]
	v_mov_b64_e32 v[64:65], v[4:5]
	s_andn2_b64 vcc, exec, s[2:3]
	v_mov_b64_e32 v[34:35], v[30:31]
	v_mov_b64_e32 v[42:43], v[26:27]
	v_mov_b64_e32 v[38:39], v[22:23]
	v_mov_b64_e32 v[46:47], v[18:19]
	v_mov_b64_e32 v[50:51], v[14:15]
	v_mov_b64_e32 v[54:55], v[10:11]
	v_mov_b64_e32 v[58:59], v[6:7]
	v_mov_b64_e32 v[62:63], v[2:3]
	s_mov_b32 s11, s27
	s_mov_b32 s25, s26
	s_mov_b64 s[0:1], s[4:5]
	s_cbranch_vccz .LBB0_120
	.p2align 6

; __device__ __forceinline__ unsigned xb_ld(unsigned* p)              { return __hip_atomic_load(p, __ATOMIC_RELAXED, __HIP_MEMORY_SCOPE_AGENT); }
; __device__ __forceinline__ void xcd_barrier_complete(unsigned* bar, unsigned x, unsigned& nloc, unsigned& nx) {
;     const unsigned G = gridDim.x * gridDim.y * gridDim.z;
;     unsigned sum, cnt, mine, sp = 0u;
;     for (;;) {
;         sum = 0u; cnt = 0u; mine = 0u;
; #pragma unroll
;         for (unsigned j = 0; j < 16; ++j) { const unsigned c = xb_ld(&bar[XB_XCNT(j)]); sum += c; cnt += (c > 0u) ? 1u : 0u; mine = (j == x) ? c : mine; }
;         if (sum == G) break;
;         __builtin_amdgcn_s_sleep(1);
;         if ((++sp & 255u) == 0u) { if (xb_ld(&bar[XB_TMO])) break; if (sp > XB_SPIN_CAP) { atomicAdd(&bar[XB_TMO], 1u); break; } }
;     }
.LBB0_125:
	s_and_b64 vcc, exec, s[42:43]
	s_cbranch_vccnz .LBB0_133
	.p2align 6

; __device__ __forceinline__ unsigned xb_ld(unsigned* p)              { return __hip_atomic_load(p, __ATOMIC_RELAXED, __HIP_MEMORY_SCOPE_AGENT); }
; #define XB_SPIN(cond, bar) do { unsigned _sp = 0; while (cond) { __builtin_amdgcn_s_sleep(1); \
;     if ((++_sp & 255u) == 0u) { if (xb_ld(&(bar)[XB_TMO])) break; if (_sp > XB_SPIN_CAP) { atomicAdd(&(bar)[XB_TMO], 1u); break; } } } } while (0)
; __device__ __forceinline__ void xcd_barrier(const XcdBarrier& b) {
;     ...
;             else XB_SPIN(xb_ld(&bar[XB_TOPGEN]) == tg, bar);
.LBB0_143:
	s_and_b64 s[16:17], exec, s[16:17]
	s_or_b64 s[12:13], s[16:17], s[12:13]
	s_andn2_b64 s[14:15], s[14:15], exec
	s_and_b64 s[16:17], s[18:19], exec
	s_or_b64 s[14:15], s[14:15], s[16:17]
	s_andn2_b64 exec, exec, s[12:13]
	s_cbranch_execz .LBB0_150
	.p2align 6

; __device__ __forceinline__ unsigned xb_ld(unsigned* p)              { return __hip_atomic_load(p, __ATOMIC_RELAXED, __HIP_MEMORY_SCOPE_AGENT); }
; #define XB_SPIN(cond, bar) do { unsigned _sp = 0; while (cond) { __builtin_amdgcn_s_sleep(1); \
;     if ((++_sp & 255u) == 0u) { if (xb_ld(&(bar)[XB_TMO])) break; if (_sp > XB_SPIN_CAP) { atomicAdd(&(bar)[XB_TMO], 1u); break; } } } } while (0)
; __device__ __forceinline__ void xcd_barrier(const XcdBarrier& b) {
;     ...
;             XB_SPIN(xb_ld(&bar[XB_XGEN(b.x)]) == gen, bar);
.LBB0_160:
	s_xor_b64 s[16:17], s[16:17], -1
	s_and_b64 s[18:19], exec, s[20:21]
	s_or_b64 s[12:13], s[18:19], s[12:13]
	s_andn2_b64 s[14:15], s[14:15], exec
	s_and_b64 s[16:17], s[16:17], exec
	s_or_b64 s[14:15], s[14:15], s[16:17]
	s_andn2_b64 exec, exec, s[12:13]
	s_cbranch_execz .LBB0_167
	.p2align 6

; #define GAS __attribute__((address_space(1)))
; __device__ __forceinline__ const GAS u32x4* y_row_ptr16(Frame& F, int row, int e, unsigned slot) {
;     const bool lat = row < NLAT; const int b = lat ? (row >> 11) : ((row - NLAT) >> 8);
;     const int T = lat ? e * 16 + b : 256 + e * 2 + (b >> 3);
;     return (const GAS u32x4*)(F.ws + WS_Y + ((size_t)T * 256 + slot) * D) + F.lane;
; __device__ __forceinline__ void rowrq_consume(Frame& F, const RowRq& R, f32x4 (&v)[4]) {
;     ...
;     while (mask) {
;         const int e = __builtin_ctzll(mask); mask &= mask - 1;
;         const u32x4 ww = *y_row_ptr16(F, R.row, e, (unsigned)__builtin_amdgcn_readlane((int)R.ts, e));
.LBB0_232:
	s_cmp_lt_i32 s44, 0x8000
	s_cselect_b64 s[2:3], -1, 0
	s_add_i32 s5, s44, 0xffff8000
	s_lshr_b32 s5, s5, 11
	s_addk_i32 s5, 0x100
	s_ashr_i32 s6, s44, 11
	.p2align 6

; #define GAS __attribute__((address_space(1)))
; __device__ __forceinline__ const GAS u32x4* y_row_ptr16(Frame& F, int row, int e, unsigned slot) {
;     const bool lat = row < NLAT; const int b = lat ? (row >> 11) : ((row - NLAT) >> 8);
;     const int T = lat ? e * 16 + b : 256 + e * 2 + (b >> 3);
;     return (const GAS u32x4*)(F.ws + WS_Y + ((size_t)T * 256 + slot) * D) + F.lane;
; __device__ __forceinline__ void rowrq_consume(Frame& F, const RowRq& R, f32x4 (&v)[4]) {
;     ...
;     while (mask) {
;         const int e = __builtin_ctzll(mask); mask &= mask - 1;
;         const u32x4 ww = *y_row_ptr16(F, R.row, e, (unsigned)__builtin_amdgcn_readlane((int)R.ts, e));
.LBB0_259:
	s_cmp_lt_i32 s40, 0x8000
	s_cselect_b64 s[2:3], -1, 0
	s_add_i32 s6, s40, 0xffff8000
	s_lshr_b32 s6, s6, 11
	s_addk_i32 s6, 0x100
	s_ashr_i32 s7, s40, 11
	.p2align 6

; __device__ __forceinline__ void rowrq_consume(Frame& F, const RowRq& R, f32x4 (&v)[4]) {
;     ...
;     while (mask) {
;         const int e = __builtin_ctzll(mask); mask &= mask - 1;
;         const u32x4 ww = *y_row_ptr16(F, R.row, e, (unsigned)__builtin_amdgcn_readlane((int)R.ts, e));
; #pragma unroll
;         for (int q = 0; q < 4; ++q) y_add4(v[q], ww[q]);
;     }
.LBB0_283:
	s_add_u32 s18, s56, -1
	s_addc_u32 s19, s57, -1
	s_and_b64 s[56:57], s[18:19], s[56:57]
	s_cmp_eq_u64 s[56:57], 0
	s_cbranch_scc1 .LBB0_285
	.p2align 6

; #define N1_STEP(RC, RI, kk) do { const int k_ = (kk), row_ = rbeg + k_; N1_MOD16(row_); N1_ISSUE(RI, k_ + 2); f32x4 v_[4]; rowrq_consume(F, RC, v_); n1_finish16(F, L, row_, v_, gs, sh); } while (0)
; __device__ __forceinline__ void rowrq_consume(Frame& F, const RowRq& R, f32x4 (&v)[4]) {
;     ...
;     while (mask) {
;         const int e = __builtin_ctzll(mask); mask &= mask - 1;
;         const u32x4 ww = *y_row_ptr16(F, R.row, e, (unsigned)__builtin_amdgcn_readlane((int)R.ts, e));
; __device__ __forceinline__ void n1_phase(const Frame& F0, int L, int nrows) {
;     ...
;         if (k < RPW) { N1_STEP(R0, R2, k); if (k + 1 < RPW) N1_STEP(R1, R0, k + 1); }
.LBB0_358:
	s_cmp_lt_i32 s40, 0x8000
	s_cselect_b64 s[2:3], -1, 0
	s_add_i32 s5, s40, 0xffff8000
	s_lshr_b32 s5, s5, 11
	s_addk_i32 s5, 0x100
	s_ashr_i32 s6, s40, 11
	.p2align 6

; #define N1_XLD(X, r) do { const GAS f32x4* xin_ = (const GAS f32x4*)N1_XIN(r) + F.lane; _Pragma("unroll") for (int j = 0; j < 4; ++j) X[j] = xin_[64 * j]; } while (0)
; #define N1_STEP0(XC, XI, kk) do { const int k_ = (kk), row_ = rbeg + k_; N1_MOD(row_); N1_XLD(XI, rbeg + (k_ + 2 < RPW ? k_ + 2 : RPW - 1)); n1_finish(F, L, row_, XC, gs, sh); } while (0)
; __device__ __forceinline__ void n1_phase(const Frame& F0, int L, int nrows) {
;     ...
;     if (L == 0) {
;     ...
;         f32x4 X0[4], X1[4], X2[4];
;         N1_XLD(X0, rbeg); N1_XLD(X1, rbeg + 1);
;         int k = 0;
;         for (; k + 2 < RPW; k += 3) { N1_STEP0(X0, X2, k); N1_STEP0(X1, X0, k + 1); N1_STEP0(X2, X1, k + 2); }
.LBB0_373:
	s_lshl_b64 s[2:3], s[2:3], 12
	s_add_u32 s0, s0, s2
	s_addc_u32 s1, s1, s3
	s_nop 1
	global_load_dwordx4 v[14:17], v84, s[0:1] nt
	global_load_dwordx4 v[10:13], v84, s[0:1] offset:1024 nt
	global_load_dwordx4 v[6:9], v84, s[0:1] offset:2048 nt
	global_load_dwordx4 v[2:5], v84, s[0:1] offset:3072 nt
	v_readlane_b32 s4, v255, 22
	s_cmp_lt_i32 s4, 3
	v_lshlrev_b32_e32 v190, 2, v1
	v_lshlrev_b32_e32 v82, 3, v1
	s_cbranch_scc1 .LBB0_395
	v_readlane_b32 s0, v252, 20
	v_mov_b32_e32 v83, v191
	v_readlane_b32 s1, v252, 21
	s_ashr_i32 s39, s38, 31
	v_mov_b32_e32 v85, v191
	v_lshl_add_u64 v[94:95], s[0:1], 0, v[82:83]
	s_lshl_b64 s[0:1], s[38:39], 10
	v_or_b32_e32 v98, s0, v190
	v_mov_b32_e32 v99, s1
	s_lshl_b64 s[0:1], s[38:39], 11
	s_mov_b32 s17, -1
	s_add_i32 s18, s4, -1
	s_mov_b32 s19, 4
	v_lshl_add_u64 v[86:87], s[28:29], 0, v[84:85]
	v_or_b32_e32 v88, 0x100, v190
	v_or_b32_e32 v90, 0x200, v190
	v_or_b32_e32 v92, 0x300, v190
	v_lshl_add_u64 v[96:97], s[96:97], 0, v[190:191]
	v_or_b32_e32 v100, s0, v82
	v_mov_b32_e32 v101, s1
	.p2align 6

; __device__ __forceinline__ unsigned xb_ld(unsigned* p)              { return __hip_atomic_load(p, __ATOMIC_RELAXED, __HIP_MEMORY_SCOPE_AGENT); }
; __device__ __forceinline__ void xcd_barrier_complete(unsigned* bar, unsigned x, unsigned& nloc, unsigned& nx) {
;     const unsigned G = gridDim.x * gridDim.y * gridDim.z;
;     unsigned sum, cnt, mine, sp = 0u;
;     for (;;) {
;         sum = 0u; cnt = 0u; mine = 0u;
; #pragma unroll
;         for (unsigned j = 0; j < 16; ++j) { const unsigned c = xb_ld(&bar[XB_XCNT(j)]); sum += c; cnt += (c > 0u) ? 1u : 0u; mine = (j == x) ? c : mine; }
;         if (sum == G) break;
;         __builtin_amdgcn_s_sleep(1);
;         if ((++sp & 255u) == 0u) { if (xb_ld(&bar[XB_TMO])) break; if (sp > XB_SPIN_CAP) { atomicAdd(&bar[XB_TMO], 1u); break; } }
;     }
.LBB0_407:
	s_and_b64 vcc, exec, s[4:5]
	s_cbranch_vccnz .LBB0_415
	.p2align 6

; __device__ __forceinline__ unsigned xb_ld(unsigned* p)              { return __hip_atomic_load(p, __ATOMIC_RELAXED, __HIP_MEMORY_SCOPE_AGENT); }
; #define XB_SPIN(cond, bar) do { unsigned _sp = 0; while (cond) { __builtin_amdgcn_s_sleep(1); \
;     if ((++_sp & 255u) == 0u) { if (xb_ld(&(bar)[XB_TMO])) break; if (_sp > XB_SPIN_CAP) { atomicAdd(&(bar)[XB_TMO], 1u); break; } } } } while (0)
; __device__ __forceinline__ void xcd_barrier(const XcdBarrier& b) {
;     ...
;             else XB_SPIN(xb_ld(&bar[XB_TOPGEN]) == tg, bar);
.LBB0_425:
	s_and_b64 s[10:11], exec, s[10:11]
	s_or_b64 s[6:7], s[10:11], s[6:7]
	s_andn2_b64 s[8:9], s[8:9], exec
	s_and_b64 s[10:11], s[18:19], exec
	s_or_b64 s[8:9], s[8:9], s[10:11]
	s_andn2_b64 exec, exec, s[6:7]
	s_cbranch_execz .LBB0_432
	.p2align 6

; __device__ __forceinline__ unsigned xb_ld(unsigned* p)              { return __hip_atomic_load(p, __ATOMIC_RELAXED, __HIP_MEMORY_SCOPE_AGENT); }
; #define XB_SPIN(cond, bar) do { unsigned _sp = 0; while (cond) { __builtin_amdgcn_s_sleep(1); \
;     if ((++_sp & 255u) == 0u) { if (xb_ld(&(bar)[XB_TMO])) break; if (_sp > XB_SPIN_CAP) { atomicAdd(&(bar)[XB_TMO], 1u); break; } } } } while (0)
; __device__ __forceinline__ void xcd_barrier(const XcdBarrier& b) {
;     ...
;             XB_SPIN(xb_ld(&bar[XB_XGEN(b.x)]) == gen, bar);
.LBB0_442:
	s_xor_b64 s[18:19], s[18:19], -1
	s_and_b64 s[10:11], exec, s[10:11]
	s_or_b64 s[6:7], s[10:11], s[6:7]
	s_andn2_b64 s[8:9], s[8:9], exec
	s_and_b64 s[10:11], s[18:19], exec
	s_or_b64 s[8:9], s[8:9], s[10:11]
	s_andn2_b64 exec, exec, s[6:7]
	s_cbranch_execz .LBB0_449
	.p2align 6

; #define GAS __attribute__((address_space(1)))
; #define LAS __attribute__((address_space(3)))
; __device__ __forceinline__ void titem_store(const TItem& T, int lane, const f32x4 (&v)[8], LAS float* scr) {
;     ...
;     for (int j = 0; j < 4; ++j) { const int n = (lane >> 3) + 8 * j; const LAS float* s = scr + (8 * c) * 33 + n;
;         if (T.f8) { u32x2 o; o.x = pg8::pack4_fp8(s[0 * 33] * pg8::SC_W, s[1 * 33] * pg8::SC_W, s[2 * 33] * pg8::SC_W, s[3 * 33] * pg8::SC_W); o.y = pg8::pack4_fp8(s[4 * 33] * pg8::SC_W, s[5 * 33] * pg8::SC_W, s[6 * 33] * pg8::SC_W, s[7 * 33] * pg8::SC_W);
;             *(GAS u32x2*)((unsigned char*)T.WT + (size_t)row_map(T.mode, n0, n) * 1024 + k0 + 8 * c) = o; }
; __device__ __forceinline__ void moe_convert_run(Frame& F, int L, int first, int end, int stride, LAS float* scr) {
;     ...
;     for (int r = first; r < end; r += stride) {
;         const TItem T = nT; f32x4 v[8];
; #pragma unroll
;         for (int i = 0; i < 8; ++i) v[i] = nv[i];
;         if (r + stride < end) { nT = moe_item(F, L, r + stride); titem_load(nT, F.lane, nv); }
;         titem_store(T, F.lane, v, scr);
;     }
.LBB0_493:
	s_waitcnt lgkmcnt(3)
	v_mul_f32_e32 v40, 0x43800000, v40
	v_mul_f32_e32 v41, 0x43800000, v41
	s_waitcnt lgkmcnt(2)
	v_mul_f32_e32 v43, 0x43800000, v38
	v_med3_f32 v40, v40, s15, v212
	v_med3_f32 v41, v41, s15, v212
	v_mov_b32_e32 v38, v191
	v_cvt_pk_fp8_f32 v38, v40, v41
	v_mul_f32_e32 v39, 0x43800000, v39
	v_med3_f32 v40, v43, s15, v212
	v_med3_f32 v39, v39, s15, v212
	s_waitcnt lgkmcnt(1)
	v_mul_f32_e32 v36, 0x43800000, v36
	v_mul_f32_e32 v37, 0x43800000, v37
	v_cvt_pk_fp8_f32 v38, v40, v39 op_sel:[0,0,1]
	v_med3_f32 v36, v36, s15, v212
	v_med3_f32 v37, v37, s15, v212
	v_mov_b32_e32 v39, v191
	v_cvt_pk_fp8_f32 v39, v36, v37
	s_waitcnt lgkmcnt(0)
	v_mul_f32_e32 v34, 0x43800000, v34
	v_mul_f32_e32 v35, 0x43800000, v35
	v_med3_f32 v34, v34, s15, v212
	v_med3_f32 v35, v35, s15, v212
	v_cvt_pk_fp8_f32 v39, v34, v35 op_sel:[0,0,1]
	v_or_b32_e32 v34, v42, v73
	v_ashrrev_i32_e32 v35, 31, v34
	v_lshlrev_b64 v[34:35], 10, v[34:35]
	v_lshl_add_u64 v[34:35], s[0:1], 0, v[34:35]
	v_lshl_add_u64 v[34:35], v[34:35], 0, s[6:7]
	v_lshl_add_u64 v[34:35], v[34:35], 0, v[66:67]
	global_store_dwordx2 v[34:35], v[38:39], off nt
	s_waitcnt lgkmcnt(0)
	s_waitcnt vmcnt(4)
	v_mov_b64_e32 v[36:37], v[32:33]
	v_mov_b64_e32 v[40:41], v[28:29]
	v_mov_b64_e32 v[44:45], v[24:25]
	v_mov_b64_e32 v[48:49], v[20:21]
	v_mov_b64_e32 v[52:53], v[16:17]
	v_mov_b64_e32 v[56:57], v[12:13]
	v_mov_b64_e32 v[60:61], v[8:9]
	v_mov_b64_e32 v[64:65], v[4:5]
	s_add_i32 s22, s22, 8
	s_andn2_b64 vcc, exec, s[2:3]
	v_mov_b64_e32 v[34:35], v[30:31]
	v_mov_b64_e32 v[38:39], v[26:27]
	v_mov_b64_e32 v[42:43], v[22:23]
	v_mov_b64_e32 v[46:47], v[18:19]
	v_mov_b64_e32 v[50:51], v[14:15]
	v_mov_b64_e32 v[54:55], v[10:11]
	v_mov_b64_e32 v[58:59], v[6:7]
	v_mov_b64_e32 v[62:63], v[2:3]
	s_mov_b32 s10, s28
	s_mov_b32 s23, s25
	s_mov_b64 s[0:1], s[4:5]
	s_cbranch_vccz .LBB0_537
	.p2align 6

; #define PHASE_FRAME(F0) Frame F = F0; { int t_ = threadIdx.x; asm volatile("" : "+v"(t_)); F.tid = t_; F.lane = t_ & 63; F.wave = __builtin_amdgcn_readfirstlane(t_ >> 6); }
; #define CV_LDU(UB, i) do { int r_ = rbeg + (i); r_ = r_ < 0 ? 0 : (r_ > rlast ? rlast : r_); UB = *(const GAS u32x4*)(U + (size_t)r_ * D); } while (0)
; #define CV_LDB(BB, i) do { const int r_ = rbeg + ((i) < RPW ? (i) : RPW - 1); BB = *(const GAS u32x4*)(BG + (size_t)r_ * D); } while (0)
; __device__ __forceinline__ void conv_phase(const Frame& F0, int jl, int nrows) {
;     PHASE_FRAME(F0);
;     const int gw = blockIdx.x * 8 + F.wave, NGW = F.G * 4, RPW = nrows / NGW, rbeg = (gw >> 1) * RPW, c0 = 512 * (gw & 1) + 8 * F.lane;
;     const bf16_t* BG = (const bf16_t*)(F.ws + WS_BG) + c0; const bf16_t* U = (const bf16_t*)(F.ws + WS_U) + c0; bf16_t* H = (bf16_t*)(F.ws + WS_H) + c0;
;     const float* ck = inp(F, I_CK) + (size_t)jl * 3 * 1024 + c0; const float* cbias = inp(F, I_CB) + (size_t)jl * 1024 + c0;
;     f32x4 k0[2], k1[2], k2[2], cb[2];
; #pragma unroll
;     for (int q = 0; q < 2; ++q) { k0[q] = *(const f32x4*)(ck + 4 * q); k1[q] = *(const f32x4*)(ck + 1024 + 4 * q); k2[q] = *(const f32x4*)(ck + 2048 + 4 * q); cb[q] = *(const f32x4*)(cbias + 4 * q); }
;     u32x4 U0, U1, U2, U3, U4, U5, B0, B1, B2, B3, B4, B5;
;     const int rlast = rbeg + RPW < nrows ? rbeg + RPW : nrows - 1;
;     ...
;     CV_LDU(U5, -1); CV_LDU(U0, 0); CV_LDU(U1, 1); CV_LDB(B0, 0); CV_LDU(U2, 2); CV_LDB(B1, 1); CV_LDU(U3, 3); CV_LDB(B2, 2);
;     int i = 0;
;     for (; i + 5 < RPW; i += 6) {
.LBB0_591:
	s_cmp_le_i32 s92, s12
	s_cselect_b64 s[0:1], -1, 0
	s_cmp_lt_i32 s12, s93
	s_cselect_b64 s[2:3], -1, 0
	s_and_b64 s[2:3], s[0:1], s[2:3]
	s_mov_b64 s[0:1], 0
	s_andn2_b64 vcc, exec, s[2:3]
	s_mov_b64 s[50:51], 0
	s_cbranch_vccnz .LBB0_655
	v_mov_b32_e32 v1, v0
	v_readlane_b32 s3, v252, 17
	v_readfirstlane_b32 s2, v1
	s_ashr_i32 s2, s2, 6
	s_add_i32 s3, s2, s3
	s_ashr_i32 s4, s3, 1
	v_readlane_b32 s3, v255, 8
	s_lshl_b32 s2, s2, 9
	v_lshlrev_b32_e32 v1, 3, v1
	s_waitcnt vmcnt(0) lgkmcnt(0)
	v_mov_b32_e32 v2, s3
	ds_read_b128 v[2:5], v2
	s_and_b32 s2, s2, 0x200
	v_and_b32_e32 v1, 0x1f8, v1
	v_or_b32_e32 v1, s2, v1
	s_mul_i32 s6, s44, 0x3000
	s_waitcnt lgkmcnt(0)
	v_readfirstlane_b32 s2, v2
	v_readfirstlane_b32 s3, v3
	s_mul_hi_u32 s5, s44, 0x3000
	s_add_u32 s2, s2, s6
	s_mov_b32 s45, s13
	s_addc_u32 s3, s3, s5
	v_lshlrev_b32_e32 v190, 2, v1
	v_lshl_add_u64 v[2:3], s[2:3], 0, v[190:191]
	v_readfirstlane_b32 s5, v4
	s_lshl_b64 s[2:3], s[44:45], 12
	v_readfirstlane_b32 s6, v5
	s_add_u32 s2, s5, s2
	s_addc_u32 s3, s6, s3
	v_lshl_add_u64 v[10:11], s[2:3], 0, v[190:191]
	s_movk_i32 s2, 0x1000
	v_add_co_u32_e32 v4, vcc, s2, v2
	s_movk_i32 s2, 0x2000
	s_nop 0
	v_addc_co_u32_e32 v5, vcc, 0, v3, vcc
	v_add_co_u32_e32 v12, vcc, s2, v2
	v_readlane_b32 s2, v254, 59
	v_readlane_b32 s8, v255, 16
	s_mul_hi_u32 s2, s8, s2
	v_readlane_b32 s7, v254, 58
	s_mul_i32 s3, s2, s7
	s_sub_i32 s3, s8, s3
	s_add_i32 s5, s2, 1
	s_sub_i32 s6, s3, s7
	s_cmp_ge_u32 s3, s7
	s_cselect_b32 s2, s5, s2
	s_cselect_b32 s3, s6, s3
	s_add_i32 s5, s2, 1
	s_cmp_ge_u32 s3, s7
	s_cselect_b32 s2, s5, s2
	v_readlane_b32 s3, v254, 63
	s_xor_b32 s2, s2, s3
	s_sub_i32 s12, s2, s3
	v_readlane_b32 s2, v252, 13
	v_lshlrev_b32_e32 v190, 1, v1
	v_readlane_b32 s3, v252, 14
	s_mul_i32 s17, s12, s4
	v_addc_co_u32_e32 v13, vcc, 0, v3, vcc
	v_lshl_add_u64 v[76:77], s[2:3], 0, v[190:191]
	v_readlane_b32 s2, v253, 32
	v_readlane_b32 s3, v253, 33
	flat_load_dwordx4 v[18:21], v[2:3]
	flat_load_dwordx4 v[14:17], v[2:3] offset:16
	flat_load_dwordx4 v[26:29], v[4:5]
	flat_load_dwordx4 v[6:9], v[4:5] offset:16
	flat_load_dwordx4 v[22:25], v[12:13]
	s_nop 0
	flat_load_dwordx4 v[2:5], v[12:13] offset:16
	flat_load_dwordx4 v[30:33], v[10:11]
	s_nop 0
	flat_load_dwordx4 v[10:13], v[10:11] offset:16
	v_lshl_add_u64 v[78:79], s[2:3], 0, v[190:191]
	s_add_i32 s2, s17, s12
	s_add_i32 s3, s8, -1
	s_min_i32 s25, s2, s3
	s_add_i32 s2, s17, -1
	s_min_i32 s2, s2, s25
	s_ashr_i32 s3, s2, 31
	s_lshl_b64 s[2:3], s[2:3], 10
	s_cmp_gt_i32 s17, 0
	s_cselect_b32 s3, s3, 0
	s_cselect_b32 s2, s2, 0
	v_lshl_add_u64 v[34:35], s[2:3], 1, v[78:79]
	s_min_i32 s2, s17, s25
	s_ashr_i32 s3, s2, 31
	s_lshl_b64 s[2:3], s[2:3], 10
	s_cmp_gt_i32 s17, -1
	s_cselect_b32 s3, s3, 0
	s_cselect_b32 s2, s2, 0
	v_lshl_add_u64 v[38:39], s[2:3], 1, v[78:79]
	s_add_i32 s2, s17, 1
	s_min_i32 s2, s2, s25
	s_ashr_i32 s3, s2, 31
	s_lshl_b64 s[2:3], s[2:3], 10
	s_cmp_gt_i32 s17, -2
	s_cselect_b32 s3, s3, 0
	s_cselect_b32 s2, s2, 0
	s_add_i32 s28, s12, -1
	global_load_dwordx4 v[34:37], v[34:35], off
	s_nop 0
	global_load_dwordx4 v[42:45], v[38:39], off
	v_lshl_add_u64 v[38:39], s[2:3], 1, v[78:79]
	s_min_i32 s2, s28, 0
	s_add_i32 s2, s2, s17
	s_ashr_i32 s3, s2, 31
	s_lshl_b64 s[2:3], s[2:3], 11
	v_lshl_add_u64 v[40:41], v[76:77], 0, s[2:3]
	s_add_i32 s2, s17, 2
	s_min_i32 s2, s2, s25
	s_ashr_i32 s3, s2, 31
	s_lshl_b64 s[2:3], s[2:3], 10
	s_cmp_gt_i32 s17, -3
	s_cselect_b32 s3, s3, 0
	s_cselect_b32 s2, s2, 0
	global_load_dwordx4 v[62:65], v[38:39], off
	global_load_dwordx4 v[58:61], v[40:41], off
	v_lshl_add_u64 v[38:39], s[2:3], 1, v[78:79]
	s_min_i32 s2, s28, 1
	s_add_i32 s2, s2, s17
	s_ashr_i32 s3, s2, 31
	s_lshl_b64 s[2:3], s[2:3], 11
	v_lshl_add_u64 v[40:41], v[76:77], 0, s[2:3]
	s_add_i32 s2, s17, 3
	s_min_i32 s2, s2, s25
	s_ashr_i32 s3, s2, 31
	s_lshl_b64 s[2:3], s[2:3], 10
	s_cmp_gt_i32 s17, -4
	s_cselect_b32 s3, s3, 0
	s_cselect_b32 s2, s2, 0
	global_load_dwordx4 v[54:57], v[38:39], off
	global_load_dwordx4 v[50:53], v[40:41], off
	v_lshl_add_u64 v[38:39], s[2:3], 1, v[78:79]
	s_min_i32 s2, s28, 2
	s_add_i32 s2, s2, s17
	s_ashr_i32 s3, s2, 31
	s_lshl_b64 s[2:3], s[2:3], 11
	v_lshl_add_u64 v[46:47], v[76:77], 0, s[2:3]
	global_load_dwordx4 v[38:41], v[38:39], off
	s_nop 0
	global_load_dwordx4 v[46:49], v[46:47], off
	s_mov_b32 s30, 0
	v_lshl_add_u64 v[74:75], s[96:97], 0, v[190:191]
	s_cmp_lt_i32 s12, 6
	s_mov_b32 s11, 5
	s_cbranch_scc1 .LBB0_595
	s_waitcnt vmcnt(0) lgkmcnt(0)
	v_mov_b32_e32 v70, v4
	v_mov_b32_e32 v71, v16
	v_mov_b32_e32 v72, v5
	v_mov_b32_e32 v73, v17
	v_mov_b32_e32 v80, v2
	v_mov_b32_e32 v81, v14
	v_mov_b32_e32 v82, v3
	v_mov_b32_e32 v83, v15
	v_mov_b32_e32 v84, v24
	v_mov_b32_e32 v85, v20
	v_mov_b32_e32 v86, v25
	v_mov_b32_e32 v87, v21
	v_mov_b32_e32 v88, v22
	v_mov_b32_e32 v89, v18
	v_mov_b32_e32 v90, v23
	v_mov_b32_e32 v91, v19
	v_mov_b32_e32 v92, v8
	v_mov_b32_e32 v93, v16
	v_mov_b32_e32 v94, v9
	v_mov_b32_e32 v95, v17
	v_mov_b32_e32 v96, v6
	v_mov_b32_e32 v97, v14
	v_mov_b32_e32 v98, v7
	v_mov_b32_e32 v99, v15
	v_mov_b32_e32 v100, v28
	v_mov_b32_e32 v101, v20
	v_mov_b32_e32 v102, v29
	v_mov_b32_e32 v103, v21
	v_mov_b32_e32 v104, v26
	v_mov_b32_e32 v105, v18
	v_mov_b32_e32 v106, v27
	v_mov_b32_e32 v107, v19
	v_mov_b32_e32 v108, v16
	v_mov_b32_e32 v109, v4
	v_mov_b32_e32 v110, v17
	v_mov_b32_e32 v111, v5
	v_mov_b32_e32 v112, v14
	v_mov_b32_e32 v113, v2
	v_mov_b32_e32 v114, v15
	v_mov_b32_e32 v115, v3
	v_mov_b32_e32 v116, v20
	v_mov_b32_e32 v117, v24
	v_mov_b32_e32 v118, v21
	v_mov_b32_e32 v119, v25
	v_mov_b32_e32 v120, v18
	v_mov_b32_e32 v121, v22
	v_mov_b32_e32 v122, v19
	v_mov_b32_e32 v123, v23
	s_movk_i32 s31, 0x7ff
	.p2align 6

; __device__ __forceinline__ unsigned xb_ld(unsigned* p)              { return __hip_atomic_load(p, __ATOMIC_RELAXED, __HIP_MEMORY_SCOPE_AGENT); }
; __device__ __forceinline__ void xcd_barrier_complete(unsigned* bar, unsigned x, unsigned& nloc, unsigned& nx) {
;     const unsigned G = gridDim.x * gridDim.y * gridDim.z;
;     unsigned sum, cnt, mine, sp = 0u;
;     for (;;) {
;         sum = 0u; cnt = 0u; mine = 0u;
; #pragma unroll
;         for (unsigned j = 0; j < 16; ++j) { const unsigned c = xb_ld(&bar[XB_XCNT(j)]); sum += c; cnt += (c > 0u) ? 1u : 0u; mine = (j == x) ? c : mine; }
;         if (sum == G) break;
;         __builtin_amdgcn_s_sleep(1);
;         if ((++sp & 255u) == 0u) { if (xb_ld(&bar[XB_TMO])) break; if (sp > XB_SPIN_CAP) { atomicAdd(&bar[XB_TMO], 1u); break; } }
;     }
.LBB0_605:
	s_and_b64 vcc, exec, s[6:7]
	s_cbranch_vccnz .LBB0_613
	.p2align 6

; __device__ __forceinline__ unsigned xb_ld(unsigned* p)              { return __hip_atomic_load(p, __ATOMIC_RELAXED, __HIP_MEMORY_SCOPE_AGENT); }
; #define XB_SPIN(cond, bar) do { unsigned _sp = 0; while (cond) { __builtin_amdgcn_s_sleep(1); \
;     if ((++_sp & 255u) == 0u) { if (xb_ld(&(bar)[XB_TMO])) break; if (_sp > XB_SPIN_CAP) { atomicAdd(&(bar)[XB_TMO], 1u); break; } } } } while (0)
; __device__ __forceinline__ void xcd_barrier(const XcdBarrier& b) {
;     ...
;             else XB_SPIN(xb_ld(&bar[XB_TOPGEN]) == tg, bar);
.LBB0_623:
	s_and_b64 s[18:19], exec, s[18:19]
	s_or_b64 s[8:9], s[18:19], s[8:9]
	s_andn2_b64 s[10:11], s[10:11], exec
	s_and_b64 s[18:19], s[22:23], exec
	s_or_b64 s[10:11], s[10:11], s[18:19]
	s_andn2_b64 exec, exec, s[8:9]
	s_cbranch_execz .LBB0_630
	.p2align 6

; __device__ __forceinline__ unsigned xb_ld(unsigned* p)              { return __hip_atomic_load(p, __ATOMIC_RELAXED, __HIP_MEMORY_SCOPE_AGENT); }
; #define XB_SPIN(cond, bar) do { unsigned _sp = 0; while (cond) { __builtin_amdgcn_s_sleep(1); \
;     if ((++_sp & 255u) == 0u) { if (xb_ld(&(bar)[XB_TMO])) break; if (_sp > XB_SPIN_CAP) { atomicAdd(&(bar)[XB_TMO], 1u); break; } } } } while (0)
; __device__ __forceinline__ void xcd_barrier(const XcdBarrier& b) {
;     ...
;             XB_SPIN(xb_ld(&bar[XB_XGEN(b.x)]) == gen, bar);
.LBB0_640:
	s_xor_b64 s[22:23], s[22:23], -1
	s_and_b64 s[18:19], exec, s[18:19]
	s_or_b64 s[8:9], s[18:19], s[8:9]
	s_andn2_b64 s[10:11], s[10:11], exec
	s_and_b64 s[18:19], s[22:23], exec
	s_or_b64 s[10:11], s[10:11], s[18:19]
	s_andn2_b64 exec, exec, s[8:9]
	s_cbranch_execz .LBB0_647
	.p2align 6

; __device__ __forceinline__ void wmask(f32x16&p0,f32x16&p1,int krel,int qrel,int hi,int wid){
;   const int dlo=krel-(32*wid+31), dhi=krel+63-32*wid;
;   if(dlo>=-128&&dhi<=128)return;
; template<int THRL> __device__ __forceinline__ void attn_unit(const AttU&U,const bf16*Q,const bf16*__restrict__ K,const bf16*__restrict__ V,bf16*O,char*shm){
;     ...
;   for(;t+1<NT;t+=2){
.LBB0_931:
	s_add_i32 s0, s9, 1
	s_cmp_ge_i32 s0, s22
	v_lshl_add_u32 v216, v206, 4, s6
	s_cbranch_scc1 .LBB0_983
	s_add_i32 s0, s4, s9
	s_lshl_b32 s1, s0, 6
	v_lshlrev_b32_e32 v82, 2, v206
	s_add_i32 s1, s1, 64
	s_sub_i32 s0, s0, s22
	v_or_b32_e32 v83, s1, v82
	s_lshl_b32 s47, s0, 6
	v_sub_u32_e32 v83, v83, v198
	v_or_b32_e32 v82, s47, v82
	v_subrev_u32_e32 v83, s23, v83
	s_lshl_b32 s2, s22, 6
	v_sub_u32_e32 v82, v82, v198
	s_sub_i32 s0, s47, s23
	v_cmp_gt_u32_e64 s[36:37], 32, v199
	s_add_i32 s42, s23, 0xffffff9e
	s_add_i32 s43, s23, 0x42
	v_subrev_u32_e32 v218, s2, v83
	s_sub_i32 s45, s1, s2
	s_sub_i32 s46, s4, s22
	s_add_i32 s8, s9, 2
	v_subrev_u32_e32 v219, s23, v82
	s_add_i32 s52, s0, 63
	.p2align 6

; #define GAS __attribute__((address_space(1)))
; __device__ __forceinline__ void n2_phase(const Frame& F0, int L, int nrows) {
;     ...
;         if (g + 1 < NG) {
; #pragma unroll
;             for (int s_ = 0; s_ < 4; ++s_) nraw[s_] = *(const GAS u32x4*)(X + (size_t)(row + 16) * D + c0 + 32 * s_);
;         }
.LBB0_1207:
	v_add_u32_e32 v2, 16, v140
	v_ashrrev_i32_e32 v3, 31, v2
	v_lshlrev_b64 v[2:3], 11, v[2:3]
	v_lshl_add_u64 v[14:15], v[84:85], 0, v[2:3]
	global_load_dwordx4 v[2:5], v[14:15], off nt
	global_load_dwordx4 v[6:9], v[14:15], off offset:64 nt
	global_load_dwordx4 v[10:13], v[14:15], off offset:128 nt
	s_nop 0
	global_load_dwordx4 v[14:17], v[14:15], off offset:192 nt
	.p2align 6

; #define LAS __attribute__((address_space(3)))
; __device__ __forceinline__ void tk_phase(const Frame& F0, bool with_ctx) {
;     ...
;             LAS int* buf = cb + 64 + ((bit >> 1) & 3) * 24;
;             if (F.lane == 0) { buf[F.wave * 3] = n1; buf[F.wave * 3 + 1] = n2; buf[F.wave * 3 + 2] = n3; }
;             __syncthreads();
;             int t1 = 0, t2 = 0, t3 = 0;
; #pragma unroll
;             for (int w = 0; w < 8; ++w) { t1 += buf[w * 3]; t2 += buf[w * 3 + 1]; t3 += buf[w * 3 + 2]; }
;             T = t3 >= 256 ? c3 : t1 >= 256 ? c1 : t2 >= 256 ? c2 : T;
;         }
.LBB0_1283:
	s_or_b64 exec, exec, s[18:19]
	v_mov_b32_e32 v5, s29
	s_waitcnt lgkmcnt(0)
	s_barrier
	ds_read_b96 v[36:38], v5 offset:256
	ds_read_b32 v18, v5 offset:276
	ds_read_b64 v[44:45], v5 offset:280
	ds_read_b128 v[6:9], v5 offset:288
	ds_read_b96 v[40:42], v5 offset:304
	ds_read_b128 v[32:35], v5 offset:336
	ds_read2_b32 v[46:47], v5 offset0:67 offset1:68
	ds_read_b32 v48, v5 offset:324
	ds_read2_b32 v[50:51], v5 offset0:79 offset1:80
	ds_read_b64 v[52:53], v5 offset:328
	s_cmp_lt_u32 s28, 3
	s_waitcnt lgkmcnt(0)
	v_add_u32_e32 v18, v18, v38
	v_add_u32_e32 v6, v18, v6
	v_add_u32_e32 v6, v6, v9
	v_add_u32_e32 v6, v6, v42
	v_add_u32_e32 v18, v47, v37
	v_add_u32_e32 v18, v18, v45
	v_add_u32_e32 v6, v6, v48
	v_add_u32_e32 v6, v6, v32
	v_add_u32_e32 v9, v6, v35
	v_add_u32_e32 v6, v46, v36
	v_add_u32_e32 v6, v6, v44
	v_add_u32_e32 v6, v6, v7
	v_add_u32_e32 v7, v18, v8
	v_add_u32_e32 v8, v7, v41
	v_add_u32_e32 v18, v6, v40
	v_add_u32_e32 v18, v18, v50
	v_add_u32_e32 v8, v8, v51
	v_add_u32_e32 v5, v8, v53
	v_add_u32_e32 v6, v18, v52
	v_add_u32_e32 v5, v5, v34
	v_add_u32_e32 v6, v6, v33
	v_cmp_lt_i32_e32 vcc, s21, v5
	s_nop 1
	v_cndmask_b32_e32 v4, v30, v4, vcc
	v_cmp_lt_i32_e32 vcc, s21, v6
	s_nop 1
	v_cndmask_b32_e32 v2, v4, v2, vcc
	v_cmp_lt_i32_e32 vcc, s21, v9
	s_nop 1
	v_cndmask_b32_e32 v30, v2, v3, vcc
	s_cbranch_scc1 .LBB0_1290
	.p2align 6

; __device__ __forceinline__ void tk_phase(const Frame& F0, bool with_ctx) {
;     ...
;         unsigned long long mq[4]; int weq = 0, leq = 0;
; #pragma unroll
;         for (int k = 0; k < 4; ++k) { mq[k] = __ballot(key[k] == T); weq += __popcll(mq[k]); leq += __popcll(mq[k] & lt); }
;         if (F.lane == 0) cb[40 + F.wave] = weq;
;         __syncthreads();
;         int eqbase = leq;
;         for (int w = 0; w < F.wave; ++w) eqbase += cb[40 + w];
.LBB0_1308:
	s_or_b64 exec, exec, s[0:1]
	v_and_b32_e32 v19, s56, v14
	v_and_b32_e32 v18, s57, v1
	v_bcnt_u32_b32 v19, v19, 0
	v_and_b32_e32 v20, s54, v14
	v_bcnt_u32_b32 v18, v18, v19
	v_and_b32_e32 v19, s55, v1
	v_bcnt_u32_b32 v20, v20, 0
	v_bcnt_u32_b32 v19, v19, v20
	v_and_b32_e32 v20, s52, v14
	v_add_u32_e32 v18, v19, v18
	v_and_b32_e32 v19, s53, v1
	v_bcnt_u32_b32 v20, v20, 0
	v_and_b32_e32 v21, s50, v14
	v_bcnt_u32_b32 v19, v19, v20
	v_and_b32_e32 v20, s51, v1
	v_bcnt_u32_b32 v21, v21, 0
	v_bcnt_u32_b32 v20, v20, v21
	v_add3_u32 v18, v18, v19, v20
	v_cndmask_b32_e64 v19, 0, 1, s[4:5]
	v_cmp_ne_u32_e64 s[48:49], 1, v19
	v_cndmask_b32_e64 v19, 0, 1, s[6:7]
	s_andn2_b64 vcc, exec, s[4:5]
	v_cmp_ne_u32_e64 s[0:1], 1, v19
	s_waitcnt lgkmcnt(0)
	s_barrier
	s_cbranch_vccnz .LBB0_1316
	s_and_b64 vcc, exec, s[0:1]
	s_cbranch_vccnz .LBB0_1313
	s_add_i32 s11, 0, 0xa0
	v_mov_b32_e32 v19, 0
	v_mov_b32_e32 v21, 0
	v_mov_b32_e32 v20, 0
	s_mov_b32 s18, s25
	.p2align 6

; __device__ __forceinline__ void tk_phase(const Frame& F0, bool with_ctx) {
;     ...
;         int eqbase = leq;
;         for (int w = 0; w < F.wave; ++w) eqbase += cb[40 + w];
.LBB0_1314:
	s_lshl_b32 s18, s22, 2
	s_add_i32 s18, s18, 0
	s_sub_i32 s11, s12, s22
	s_addk_i32 s18, 0xa0
	.p2align 6

; __device__ __forceinline__ void tk_phase(const Frame& F0, bool with_ctx) {
;     ...
;         unsigned long long ms[4]; int wsel = 0, lsel = 0;
; #pragma unroll
;         for (int k = 0; k < 4; ++k) { ms[k] = __ballot(sel[k]); wsel += __popcll(ms[k]); lsel += __popcll(ms[k] & lt); }
;         if (F.lane == 0) cb[48 + F.wave] = wsel;
;         __syncthreads();
;         int slot = lsel;
;         for (int w = 0; w < F.wave; ++w) slot += cb[48 + w];
.LBB0_1318:
	s_or_b64 exec, exec, s[34:35]
	v_and_b32_e32 v3, s44, v14
	v_and_b32_e32 v2, s45, v1
	v_bcnt_u32_b32 v3, v3, 0
	v_and_b32_e32 v4, s42, v14
	v_bcnt_u32_b32 v2, v2, v3
	v_and_b32_e32 v3, s43, v1
	v_bcnt_u32_b32 v4, v4, 0
	v_bcnt_u32_b32 v3, v3, v4
	v_and_b32_e32 v4, s40, v14
	v_add_u32_e32 v2, v3, v2
	v_and_b32_e32 v3, s41, v1
	v_bcnt_u32_b32 v4, v4, 0
	v_and_b32_e32 v5, vcc_lo, v14
	v_bcnt_u32_b32 v3, v3, v4
	v_and_b32_e32 v4, vcc_hi, v1
	v_bcnt_u32_b32 v5, v5, 0
	v_bcnt_u32_b32 v4, v4, v5
	v_add3_u32 v2, v2, v3, v4
	s_and_b64 vcc, exec, s[48:49]
	s_waitcnt lgkmcnt(0)
	s_barrier
	s_cbranch_vccnz .LBB0_1326
	s_and_b64 vcc, exec, s[0:1]
	s_cbranch_vccnz .LBB0_1323
	s_add_i32 s0, 0, 0xc0
	v_mov_b32_e32 v3, 0
	v_mov_b32_e32 v5, 0
	v_mov_b32_e32 v4, 0
	s_mov_b32 s1, s25
	.p2align 6

; __device__ __forceinline__ void tk_phase(const Frame& F0, bool with_ctx) {
;     ...
;         int slot = lsel;
;         for (int w = 0; w < F.wave; ++w) slot += cb[48 + w];
.LBB0_1324:
	s_lshl_b32 s1, s11, 2
	s_add_i32 s1, s1, 0
	s_sub_i32 s0, s12, s11
	s_addk_i32 s1, 0xc0
	.p2align 6

; #define GAS __attribute__((address_space(1)))
; __device__ __forceinline__ const GAS u32x4* y_row_ptr16(Frame& F, int row, int e, unsigned slot) {
;     const bool lat = row < NLAT; const int b = lat ? (row >> 11) : ((row - NLAT) >> 8);
;     const int T = lat ? e * 16 + b : 256 + e * 2 + (b >> 3);
;     return (const GAS u32x4*)(F.ws + WS_Y + ((size_t)T * 256 + slot) * D) + F.lane;
; __device__ __forceinline__ void rowrq_consume(Frame& F, const RowRq& R, f32x4 (&v)[4]) {
;     ...
;     while (mask) {
;         const int e = __builtin_ctzll(mask); mask &= mask - 1;
;         const u32x4 ww = *y_row_ptr16(F, R.row, e, (unsigned)__builtin_amdgcn_readlane((int)R.ts, e));
.LBB0_1661:
	s_cmp_lt_i32 s6, 0x8000
	s_cselect_b64 s[40:41], -1, 0
	s_add_i32 s7, s6, 0xffff8000
	s_lshr_b32 s7, s7, 11
	s_addk_i32 s7, 0x100
	s_ashr_i32 s6, s6, 11
	.p2align 6

; #define GAS __attribute__((address_space(1)))
; __device__ __forceinline__ const GAS u32x4* y_row_ptr16(Frame& F, int row, int e, unsigned slot) {
;     const bool lat = row < NLAT; const int b = lat ? (row >> 11) : ((row - NLAT) >> 8);
;     const int T = lat ? e * 16 + b : 256 + e * 2 + (b >> 3);
;     return (const GAS u32x4*)(F.ws + WS_Y + ((size_t)T * 256 + slot) * D) + F.lane;
; __device__ __forceinline__ void rowrq_consume(Frame& F, const RowRq& R, f32x4 (&v)[4]) {
;     ...
;     while (mask) {
;         const int e = __builtin_ctzll(mask); mask &= mask - 1;
;         const u32x4 ww = *y_row_ptr16(F, R.row, e, (unsigned)__builtin_amdgcn_readlane((int)R.ts, e));
.LBB0_1682:
	s_cmp_lt_i32 s4, 0x8000
	s_cselect_b64 s[58:59], -1, 0
	s_add_i32 s5, s4, 0xffff8000
	s_lshr_b32 s5, s5, 11
	s_addk_i32 s5, 0x100
	s_ashr_i32 s4, s4, 11
	.p2align 6

; __device__ __forceinline__ void rowrq_consume(Frame& F, const RowRq& R, f32x4 (&v)[4]) {
;     ...
;     while (mask) {
;         const int e = __builtin_ctzll(mask); mask &= mask - 1;
;         const u32x4 ww = *y_row_ptr16(F, R.row, e, (unsigned)__builtin_amdgcn_readlane((int)R.ts, e));
; #pragma unroll
;         for (int q = 0; q < 4; ++q) y_add4(v[q], ww[q]);
;     }
.LBB0_1702:
	s_add_u32 s20, s18, -1
	s_addc_u32 s21, s19, -1
	s_and_b64 s[18:19], s[20:21], s[18:19]
	s_cmp_eq_u64 s[18:19], 0
	s_cbranch_scc1 .LBB0_1704
	.p2align 6

; __device__ __forceinline__ void y_add4(f32x4& v, unsigned w) {
;     constexpr float r = 1.0f / pg8::SC_Y;
;     v[0] += __builtin_amdgcn_cvt_f32_fp8((int)w, 0) * r; v[1] += __builtin_amdgcn_cvt_f32_fp8((int)w, 1) * r; v[2] += __builtin_amdgcn_cvt_f32_fp8((int)w, 2) * r; v[3] += __builtin_amdgcn_cvt_f32_fp8((int)w, 3) * r;
; __device__ __forceinline__ void rowrq_consume(Frame& F, const RowRq& R, f32x4 (&v)[4]) {
;     ...
;     while (mask) {
;         const int e = __builtin_ctzll(mask); mask &= mask - 1;
;         const u32x4 ww = *y_row_ptr16(F, R.row, e, (unsigned)__builtin_amdgcn_readlane((int)R.ts, e));
; #pragma unroll
;         for (int q = 0; q < 4; ++q) y_add4(v[q], ww[q]);
;     }
.LBB0_1740:
	s_cmp_lt_i32 s6, 0x8000
	s_cselect_b64 s[0:1], -1, 0
	s_add_i32 s3, s6, 0xffff8000
	s_lshr_b32 s12, s3, 11
	s_addk_i32 s12, 0x100
	s_ashr_i32 s13, s6, 11
	s_mov_b32 s7, 0
	s_mov_b32 s10, 0x3c800000
	.p2align 6

; __device__ __forceinline__ void y_add4(f32x4& v, unsigned w) {
;     constexpr float r = 1.0f / pg8::SC_Y;
;     v[0] += __builtin_amdgcn_cvt_f32_fp8((int)w, 0) * r; v[1] += __builtin_amdgcn_cvt_f32_fp8((int)w, 1) * r; v[2] += __builtin_amdgcn_cvt_f32_fp8((int)w, 2) * r; v[3] += __builtin_amdgcn_cvt_f32_fp8((int)w, 3) * r;
; __device__ __forceinline__ void rowrq_consume(Frame& F, const RowRq& R, f32x4 (&v)[4]) {
;     ...
;     while (mask) {
;         const int e = __builtin_ctzll(mask); mask &= mask - 1;
;         const u32x4 ww = *y_row_ptr16(F, R.row, e, (unsigned)__builtin_amdgcn_readlane((int)R.ts, e));
; #pragma unroll
;         for (int q = 0; q < 4; ++q) y_add4(v[q], ww[q]);
;     }
.LBB0_1760:
	s_cmp_lt_i32 s4, 0x8000
	s_cselect_b64 s[0:1], -1, 0
	s_add_i32 s3, s4, 0xffff8000
	s_lshr_b32 s10, s3, 11
	s_addk_i32 s10, 0x100
	s_ashr_i32 s11, s4, 11
	s_mov_b32 s5, 0
	s_mov_b32 s6, 0x3c800000
	.p2align 6
